# router row pass: hand-written top-4 stage (two rows per wave handled in one 32-lane-per-row arg-max chain, DPP+permlane16 max, batched partial-logit reads)
# speedup vs baseline: 1.0021x; 1.0021x over previous
.LBB0_1541:
	s_or_b64 exec, exec, s[12:13]
	s_mov_b32 s12, 28
	s_ashr_i32 s13, s12, 31
	s_lshl_b64 s[12:13], s[12:13], 3
	s_add_u32 s12, s0, s12
	s_addc_u32 s13, s1, s13
	s_load_dwordx2 s[12:13], s[12:13], 0x0
	v_and_b32_e32 v139, 31, v147
	v_lshl_or_b32 v0, s73, 5, v139
	s_andn2_b64 vcc, exec, s[14:15]
	s_waitcnt lgkmcnt(0)
	v_lshl_add_u64 v[2:3], v[0:1], 2, s[12:13]
	global_load_dword v148, v[2:3], off
	s_mov_b32 s12, 7
	s_cbranch_vccnz .LBB0_1553
	s_waitcnt vmcnt(15)
	v_cvt_pk_bf16_f32 v2, v12, v13
	v_lshlrev_b32_e32 v4, 16, v2
	v_and_b32_e32 v5, 0xffff0000, v2
	v_pk_add_f32 v[4:5], v[12:13], v[4:5] neg_lo:[0,1] neg_hi:[0,1]
	v_cvt_pk_bf16_f32 v3, v14, v15
	v_cvt_pk_bf16_f32 v6, v4, v5
	v_lshlrev_b32_e32 v4, 16, v3
	v_and_b32_e32 v5, 0xffff0000, v3
	v_pk_add_f32 v[4:5], v[14:15], v[4:5] neg_lo:[0,1] neg_hi:[0,1]
	s_ashr_i32 s13, s12, 31
	v_cvt_pk_bf16_f32 v7, v4, v5
	v_cvt_pk_bf16_f32 v4, v8, v9
	v_lshlrev_b32_e32 v12, 16, v4
	v_and_b32_e32 v13, 0xffff0000, v4
	v_cvt_pk_bf16_f32 v5, v10, v11
	v_pk_add_f32 v[8:9], v[8:9], v[12:13] neg_lo:[0,1] neg_hi:[0,1]
	v_lshlrev_b32_e32 v12, 16, v5
	v_and_b32_e32 v13, 0xffff0000, v5
	v_pk_add_f32 v[10:11], v[10:11], v[12:13] neg_lo:[0,1] neg_hi:[0,1]
	v_cvt_pk_bf16_f32 v8, v8, v9
	v_cvt_pk_bf16_f32 v9, v10, v11
	s_waitcnt vmcnt(13)
	v_cvt_pk_bf16_f32 v10, v20, v21
	v_lshlrev_b32_e32 v12, 16, v10
	v_and_b32_e32 v13, 0xffff0000, v10
	v_pk_add_f32 v[12:13], v[20:21], v[12:13] neg_lo:[0,1] neg_hi:[0,1]
	v_cvt_pk_bf16_f32 v11, v22, v23
	v_cvt_pk_bf16_f32 v14, v12, v13
	v_lshlrev_b32_e32 v12, 16, v11
	v_and_b32_e32 v13, 0xffff0000, v11
	v_pk_add_f32 v[12:13], v[22:23], v[12:13] neg_lo:[0,1] neg_hi:[0,1]
	s_lshl_b32 s70, s73, 10
	v_cvt_pk_bf16_f32 v15, v12, v13
	v_cvt_pk_bf16_f32 v12, v16, v17
	v_lshlrev_b32_e32 v20, 16, v12
	v_and_b32_e32 v21, 0xffff0000, v12
	v_cvt_pk_bf16_f32 v13, v18, v19
	v_pk_add_f32 v[16:17], v[16:17], v[20:21] neg_lo:[0,1] neg_hi:[0,1]
	v_lshlrev_b32_e32 v20, 16, v13
	v_and_b32_e32 v21, 0xffff0000, v13
	v_pk_add_f32 v[18:19], v[18:19], v[20:21] neg_lo:[0,1] neg_hi:[0,1]
	v_cvt_pk_bf16_f32 v16, v16, v17
	v_cvt_pk_bf16_f32 v17, v18, v19
	s_waitcnt vmcnt(11)
	v_cvt_pk_bf16_f32 v18, v28, v29
	v_lshlrev_b32_e32 v20, 16, v18
	v_and_b32_e32 v21, 0xffff0000, v18
	v_pk_add_f32 v[20:21], v[28:29], v[20:21] neg_lo:[0,1] neg_hi:[0,1]
	v_cvt_pk_bf16_f32 v19, v30, v31
	v_cvt_pk_bf16_f32 v22, v20, v21
	v_lshlrev_b32_e32 v20, 16, v19
	v_and_b32_e32 v21, 0xffff0000, v19
	v_pk_add_f32 v[20:21], v[30:31], v[20:21] neg_lo:[0,1] neg_hi:[0,1]
	s_lshl_b64 s[12:13], s[12:13], 3
	v_cvt_pk_bf16_f32 v23, v20, v21
	v_cvt_pk_bf16_f32 v20, v24, v25
	v_lshlrev_b32_e32 v28, 16, v20
	v_and_b32_e32 v29, 0xffff0000, v20
	v_cvt_pk_bf16_f32 v21, v26, v27
	v_pk_add_f32 v[24:25], v[24:25], v[28:29] neg_lo:[0,1] neg_hi:[0,1]
	v_lshlrev_b32_e32 v28, 16, v21
	v_and_b32_e32 v29, 0xffff0000, v21
	v_pk_add_f32 v[26:27], v[26:27], v[28:29] neg_lo:[0,1] neg_hi:[0,1]
	v_cvt_pk_bf16_f32 v24, v24, v25
	v_cvt_pk_bf16_f32 v25, v26, v27
	s_waitcnt vmcnt(9)
	v_cvt_pk_bf16_f32 v26, v36, v37
	v_lshlrev_b32_e32 v28, 16, v26
	v_and_b32_e32 v29, 0xffff0000, v26
	v_pk_add_f32 v[28:29], v[36:37], v[28:29] neg_lo:[0,1] neg_hi:[0,1]
	v_cvt_pk_bf16_f32 v27, v38, v39
	v_cvt_pk_bf16_f32 v30, v28, v29
	v_lshlrev_b32_e32 v28, 16, v27
	v_and_b32_e32 v29, 0xffff0000, v27
	v_pk_add_f32 v[28:29], v[38:39], v[28:29] neg_lo:[0,1] neg_hi:[0,1]
	s_add_u32 s12, s0, s12
	v_cvt_pk_bf16_f32 v31, v28, v29
	v_cvt_pk_bf16_f32 v28, v32, v33
	v_lshlrev_b32_e32 v36, 16, v28
	v_and_b32_e32 v37, 0xffff0000, v28
	v_cvt_pk_bf16_f32 v29, v34, v35
	v_pk_add_f32 v[32:33], v[32:33], v[36:37] neg_lo:[0,1] neg_hi:[0,1]
	v_lshlrev_b32_e32 v36, 16, v29
	v_and_b32_e32 v37, 0xffff0000, v29
	v_pk_add_f32 v[34:35], v[34:35], v[36:37] neg_lo:[0,1] neg_hi:[0,1]
	v_cvt_pk_bf16_f32 v32, v32, v33
	v_cvt_pk_bf16_f32 v33, v34, v35
	s_waitcnt vmcnt(7)
	v_cvt_pk_bf16_f32 v34, v44, v45
	v_lshlrev_b32_e32 v36, 16, v34
	v_and_b32_e32 v37, 0xffff0000, v34
	v_pk_add_f32 v[36:37], v[44:45], v[36:37] neg_lo:[0,1] neg_hi:[0,1]
	v_cvt_pk_bf16_f32 v35, v46, v47
	v_cvt_pk_bf16_f32 v38, v36, v37
	v_lshlrev_b32_e32 v36, 16, v35
	v_and_b32_e32 v37, 0xffff0000, v35
	v_pk_add_f32 v[36:37], v[46:47], v[36:37] neg_lo:[0,1] neg_hi:[0,1]
	s_addc_u32 s13, s1, s13
	v_cvt_pk_bf16_f32 v39, v36, v37
	v_cvt_pk_bf16_f32 v36, v40, v41
	v_lshlrev_b32_e32 v44, 16, v36
	v_and_b32_e32 v45, 0xffff0000, v36
	v_cvt_pk_bf16_f32 v37, v42, v43
	v_pk_add_f32 v[40:41], v[40:41], v[44:45] neg_lo:[0,1] neg_hi:[0,1]
	v_lshlrev_b32_e32 v44, 16, v37
	v_and_b32_e32 v45, 0xffff0000, v37
	v_pk_add_f32 v[42:43], v[42:43], v[44:45] neg_lo:[0,1] neg_hi:[0,1]
	v_cvt_pk_bf16_f32 v40, v40, v41
	v_cvt_pk_bf16_f32 v41, v42, v43
	s_waitcnt vmcnt(5)
	v_cvt_pk_bf16_f32 v42, v52, v53
	v_lshlrev_b32_e32 v44, 16, v42
	v_and_b32_e32 v45, 0xffff0000, v42
	v_pk_add_f32 v[44:45], v[52:53], v[44:45] neg_lo:[0,1] neg_hi:[0,1]
	v_cvt_pk_bf16_f32 v43, v54, v55
	v_cvt_pk_bf16_f32 v46, v44, v45
	v_lshlrev_b32_e32 v44, 16, v43
	v_and_b32_e32 v45, 0xffff0000, v43
	v_pk_add_f32 v[44:45], v[54:55], v[44:45] neg_lo:[0,1] neg_hi:[0,1]
	s_load_dwordx2 s[12:13], s[12:13], 0x0
	v_cvt_pk_bf16_f32 v47, v44, v45
	v_cvt_pk_bf16_f32 v44, v48, v49
	v_lshlrev_b32_e32 v52, 16, v44
	v_and_b32_e32 v53, 0xffff0000, v44
	v_cvt_pk_bf16_f32 v45, v50, v51
	v_pk_add_f32 v[48:49], v[48:49], v[52:53] neg_lo:[0,1] neg_hi:[0,1]
	v_lshlrev_b32_e32 v52, 16, v45
	v_and_b32_e32 v53, 0xffff0000, v45
	v_pk_add_f32 v[50:51], v[50:51], v[52:53] neg_lo:[0,1] neg_hi:[0,1]
	v_cvt_pk_bf16_f32 v48, v48, v49
	v_cvt_pk_bf16_f32 v49, v50, v51
	s_waitcnt vmcnt(3)
	v_cvt_pk_bf16_f32 v50, v60, v61
	v_lshlrev_b32_e32 v52, 16, v50
	v_and_b32_e32 v53, 0xffff0000, v50
	v_pk_add_f32 v[52:53], v[60:61], v[52:53] neg_lo:[0,1] neg_hi:[0,1]
	v_cvt_pk_bf16_f32 v51, v62, v63
	v_cvt_pk_bf16_f32 v54, v52, v53
	v_lshlrev_b32_e32 v52, 16, v51
	v_and_b32_e32 v53, 0xffff0000, v51
	v_pk_add_f32 v[52:53], v[62:63], v[52:53] neg_lo:[0,1] neg_hi:[0,1]
	s_lshl_b64 s[14:15], s[70:71], 2
	v_cvt_pk_bf16_f32 v55, v52, v53
	v_cvt_pk_bf16_f32 v52, v56, v57
	v_lshlrev_b32_e32 v60, 16, v52
	v_and_b32_e32 v61, 0xffff0000, v52
	v_cvt_pk_bf16_f32 v53, v58, v59
	v_pk_add_f32 v[56:57], v[56:57], v[60:61] neg_lo:[0,1] neg_hi:[0,1]
	v_lshlrev_b32_e32 v60, 16, v53
	v_and_b32_e32 v61, 0xffff0000, v53
	v_pk_add_f32 v[58:59], v[58:59], v[60:61] neg_lo:[0,1] neg_hi:[0,1]
	v_cvt_pk_bf16_f32 v56, v56, v57
	v_cvt_pk_bf16_f32 v57, v58, v59
	s_waitcnt vmcnt(1)
	v_cvt_pk_bf16_f32 v58, v68, v69
	v_lshlrev_b32_e32 v60, 16, v58
	v_and_b32_e32 v61, 0xffff0000, v58
	v_pk_add_f32 v[60:61], v[68:69], v[60:61] neg_lo:[0,1] neg_hi:[0,1]
	v_cvt_pk_bf16_f32 v59, v70, v71
	v_cvt_pk_bf16_f32 v62, v60, v61
	v_lshlrev_b32_e32 v60, 16, v59
	v_and_b32_e32 v61, 0xffff0000, v59
	v_pk_add_f32 v[60:61], v[70:71], v[60:61] neg_lo:[0,1] neg_hi:[0,1]
	s_waitcnt lgkmcnt(0)
	s_add_u32 s12, s12, s14
	v_cvt_pk_bf16_f32 v63, v60, v61
	v_cvt_pk_bf16_f32 v60, v64, v65
	v_lshlrev_b32_e32 v68, 16, v60
	v_and_b32_e32 v69, 0xffff0000, v60
	v_cvt_pk_bf16_f32 v61, v66, v67
	v_pk_add_f32 v[64:65], v[64:65], v[68:69] neg_lo:[0,1] neg_hi:[0,1]
	v_lshlrev_b32_e32 v68, 16, v61
	v_and_b32_e32 v69, 0xffff0000, v61
	v_pk_add_f32 v[66:67], v[66:67], v[68:69] neg_lo:[0,1] neg_hi:[0,1]
	v_mov_b32_e32 v73, v1
	v_lshlrev_b32_e32 v0, 4, v147
	v_cvt_pk_bf16_f32 v64, v64, v65
	v_cvt_pk_bf16_f32 v65, v66, v67
	s_addc_u32 s13, s13, s15
	v_lshl_add_u64 v[140:141], s[8:9], 0, v[72:73]
	v_lshl_add_u64 v[66:67], s[10:11], 0, v[0:1]
	s_mov_b64 s[8:9], 0x5f000000
	s_lshl_b32 s22, s16, 8
	v_lshl_add_u64 v[142:143], v[66:67], 0, s[8:9]
	s_add_i32 s8, s22, 0
	v_and_b32_e32 v66, 15, v74
	v_mov_b32_e32 v0, s8
	s_movk_i32 s8, 0x810
	s_lshl_b32 s14, s16, 1
	v_mad_u32_u24 v69, v66, s8, v0
	v_lshlrev_b32_e32 v0, 6, v147
	v_readlane_b32 s15, v254, 62
	v_lshl_add_u64 v[144:145], s[12:13], 0, v[0:1]
	s_or_b32 s12, s14, 1
	s_lshl_b32 s13, s16, 11
	v_lshlrev_b32_e32 v0, 5, v74
	s_mul_i32 s24, s12, 0x810
	v_and_b32_e32 v0, 0x600, v0
	s_add_i32 s13, s15, s13
	s_lshl_b32 s25, s12, 7
	v_readlane_b32 s12, v254, 12
	v_add_u32_e32 v75, s13, v0
	s_mul_i32 s12, s12, s17
	s_lshl_b32 s13, s18, 4
	v_lshlrev_b32_e32 v68, 2, v147
	v_and_b32_e32 v67, 48, v74
	v_lshlrev_b32_e32 v74, 2, v66
	s_add_i32 s12, s12, s13
	v_mov_b32_e32 v66, 0
	v_add_u32_e32 v149, 0, v72
	v_lshl_add_u32 v150, v147, 2, s15
	v_cmp_gt_u32_e64 s[8:9], 2, v147
	v_cmp_eq_u32_e64 s[10:11], 1, v147
	s_mul_i32 s23, s16, 0x1020
	s_add_i32 s26, s12, s14
	s_mov_b32 s27, 0
	s_mov_b32 s28, -1
	v_mov_b32_e32 v153, -1
	v_mov_b32_e32 v70, 0
	v_mov_b32_e32 v71, 0
	v_mov_b32_e32 v72, 0
	v_mov_b32_e32 v73, 0
	v_lshlrev_b32_e32 v0, 4, v68
	v_add_u32_e32 v151, v69, v67
	v_add_u32_e32 v152, v75, v74
	v_mov_b32_e32 v67, v66
	v_mov_b32_e32 v68, v66
	v_mov_b32_e32 v69, v66

.LBB0_1549:
	s_or_b64 exec, exec, s[12:13]
	s_waitcnt lgkmcnt(0)
	s_barrier
	ds_read_b128 v[122:125], v151
	ds_read_b128 v[126:129], v151 offset:33024
	s_waitcnt lgkmcnt(1)
	v_mfma_f32_16x16x32_bf16 v[130:133], v[122:125], v[2:5], 0
	v_mfma_f32_16x16x32_bf16 v[134:137], v[122:125], v[10:13], 0
	v_mfma_f32_16x16x32_bf16 v[130:133], v[122:125], v[6:9], v[130:133]
	v_mfma_f32_16x16x32_bf16 v[122:125], v[122:125], v[14:17], v[134:137]
	s_waitcnt lgkmcnt(0)
	v_mfma_f32_16x16x32_bf16 v[130:133], v[126:129], v[2:5], v[130:133]
	v_mfma_f32_16x16x32_bf16 v[122:125], v[126:129], v[10:13], v[122:125]
	ds_read_b128 v[126:129], v151 offset:64
	s_nop 1
	ds_read_b128 v[134:137], v151 offset:33088
	s_waitcnt lgkmcnt(1)
	v_mfma_f32_16x16x32_bf16 v[130:133], v[126:129], v[18:21], v[130:133]
	v_mfma_f32_16x16x32_bf16 v[122:125], v[126:129], v[26:29], v[122:125]
	v_mfma_f32_16x16x32_bf16 v[130:133], v[126:129], v[22:25], v[130:133]
	v_mfma_f32_16x16x32_bf16 v[122:125], v[126:129], v[30:33], v[122:125]
	s_waitcnt lgkmcnt(0)
	v_mfma_f32_16x16x32_bf16 v[130:133], v[134:137], v[18:21], v[130:133]
	v_mfma_f32_16x16x32_bf16 v[122:125], v[134:137], v[26:29], v[122:125]
	ds_read_b128 v[126:129], v151 offset:128
	ds_read_b128 v[134:137], v151 offset:33152
	s_waitcnt lgkmcnt(1)
	v_mfma_f32_16x16x32_bf16 v[130:133], v[126:129], v[34:37], v[130:133]
	v_mfma_f32_16x16x32_bf16 v[122:125], v[126:129], v[42:45], v[122:125]
	v_mfma_f32_16x16x32_bf16 v[130:133], v[126:129], v[38:41], v[130:133]
	v_mfma_f32_16x16x32_bf16 v[122:125], v[126:129], v[46:49], v[122:125]
	s_waitcnt lgkmcnt(0)
	v_mfma_f32_16x16x32_bf16 v[130:133], v[134:137], v[34:37], v[130:133]
	v_mfma_f32_16x16x32_bf16 v[122:125], v[134:137], v[42:45], v[122:125]
	ds_read_b128 v[126:129], v151 offset:192
	ds_read_b128 v[134:137], v151 offset:33216
	s_waitcnt lgkmcnt(1)
	v_mfma_f32_16x16x32_bf16 v[130:133], v[126:129], v[50:53], v[130:133]
	v_mfma_f32_16x16x32_bf16 v[122:125], v[126:129], v[58:61], v[122:125]
	v_mfma_f32_16x16x32_bf16 v[130:133], v[126:129], v[54:57], v[130:133]
	v_mfma_f32_16x16x32_bf16 v[122:125], v[126:129], v[62:65], v[122:125]
	v_mov_b32_e32 v126, v1
	v_mov_b32_e32 v127, v1
	v_add_u32_e32 v128, s25, v150
	s_waitcnt lgkmcnt(0)
	v_mfma_f32_16x16x32_bf16 v[130:133], v[134:137], v[50:53], v[130:133]
	v_mfma_f32_16x16x32_bf16 v[122:125], v[134:137], v[58:61], v[122:125]
	s_nop 7
	ds_write2_b32 v152, v130, v122 offset1:16
	ds_write2_b32 v152, v131, v123 offset0:32 offset1:48
	ds_write2_b32 v152, v132, v124 offset0:64 offset1:80
	ds_write2_b32 v152, v133, v125 offset0:96 offset1:112
	v_add_u32_e32 v124, s22, v150
	s_waitcnt lgkmcnt(0)
	s_barrier
	ds_read2st64_b32 v[122:123], v124 offset1:8
	ds_read2st64_b32 v[126:127], v124 offset0:16 offset1:24
	ds_read2st64_b32 v[128:129], v124 offset0:32 offset1:40
	ds_read2st64_b32 v[130:131], v124 offset0:48 offset1:56
	s_waitcnt lgkmcnt(3)
	v_add_f32_e32 v122, v148, v122
	v_add_f32_e32 v122, v122, v123
	s_waitcnt lgkmcnt(2)
	v_add_f32_e32 v122, v122, v126
	v_add_f32_e32 v122, v122, v127
	s_waitcnt lgkmcnt(1)
	v_add_f32_e32 v122, v122, v128
	v_add_f32_e32 v122, v122, v129
	s_waitcnt lgkmcnt(0)
	v_add_f32_e32 v122, v122, v130
	v_add_f32_e32 v122, v122, v131
	s_nop 1
	v_max_f32_dpp v123, v122, v122 quad_perm:[1,0,3,2] row_mask:0xf bank_mask:0xf
	s_nop 1
	v_max_f32_dpp v123, v123, v123 quad_perm:[2,3,0,1] row_mask:0xf bank_mask:0xf
	s_nop 1
	v_max_f32_dpp v123, v123, v123 row_half_mirror row_mask:0xf bank_mask:0xf
	s_nop 1
	v_max_f32_dpp v123, v123, v123 row_mirror row_mask:0xf bank_mask:0xf
	v_mov_b32_e32 v125, v123
	s_nop 1
	v_permlane16_swap_b32 v123, v125
	s_nop 1
	v_max_f32_e32 v126, v123, v125
	v_cmp_eq_f32_e32 vcc, v122, v126
	s_nop 0
	s_ff1_i32_b32 s17, vcc_lo
	s_ff1_i32_b32 s31, vcc_hi
	s_lshl_b32 s36, 1, s17
	s_lshl_b32 s37, 1, s31
	s_nop 0
	v_cndmask_b32_e64 v122, v122, v220, s[36:37]
	s_nop 1
	v_max_f32_dpp v123, v122, v122 quad_perm:[1,0,3,2] row_mask:0xf bank_mask:0xf
	s_nop 1
	v_max_f32_dpp v123, v123, v123 quad_perm:[2,3,0,1] row_mask:0xf bank_mask:0xf
	s_nop 1
	v_max_f32_dpp v123, v123, v123 row_half_mirror row_mask:0xf bank_mask:0xf
	s_nop 1
	v_max_f32_dpp v123, v123, v123 row_mirror row_mask:0xf bank_mask:0xf
	v_mov_b32_e32 v125, v123
	s_nop 1
	v_permlane16_swap_b32 v123, v125
	s_nop 1
	v_max_f32_e32 v127, v123, v125
	v_cmp_eq_f32_e32 vcc, v122, v127
	s_nop 0
	s_ff1_i32_b32 s29, vcc_lo
	s_ff1_i32_b32 s34, vcc_hi
	s_lshl_b32 s36, 1, s29
	s_lshl_b32 s37, 1, s34
	s_nop 0
	v_cndmask_b32_e64 v122, v122, v220, s[36:37]
	s_nop 1
	v_max_f32_dpp v123, v122, v122 quad_perm:[1,0,3,2] row_mask:0xf bank_mask:0xf
	s_nop 1
	v_max_f32_dpp v123, v123, v123 quad_perm:[2,3,0,1] row_mask:0xf bank_mask:0xf
	s_nop 1
	v_max_f32_dpp v123, v123, v123 row_half_mirror row_mask:0xf bank_mask:0xf
	s_nop 1
	v_max_f32_dpp v123, v123, v123 row_mirror row_mask:0xf bank_mask:0xf
	v_mov_b32_e32 v125, v123
	s_nop 1
	v_permlane16_swap_b32 v123, v125
	s_nop 1
	v_max_f32_e32 v128, v123, v125
	v_cmp_eq_f32_e32 vcc, v122, v128
	s_nop 0
	s_ff1_i32_b32 s30, vcc_lo
	s_ff1_i32_b32 s35, vcc_hi
	s_lshl_b32 s36, 1, s30
	s_lshl_b32 s37, 1, s35
	s_nop 0
	v_cndmask_b32_e64 v122, v122, v220, s[36:37]
	s_nop 1
	v_max_f32_dpp v123, v122, v122 quad_perm:[1,0,3,2] row_mask:0xf bank_mask:0xf
	s_nop 1
	v_max_f32_dpp v123, v123, v123 quad_perm:[2,3,0,1] row_mask:0xf bank_mask:0xf
	s_nop 1
	v_max_f32_dpp v123, v123, v123 row_half_mirror row_mask:0xf bank_mask:0xf
	s_nop 1
	v_max_f32_dpp v123, v123, v123 row_mirror row_mask:0xf bank_mask:0xf
	v_mov_b32_e32 v125, v123
	s_nop 1
	v_permlane16_swap_b32 v123, v125
	s_nop 1
	v_max_f32_e32 v129, v123, v125
	v_cmp_eq_f32_e32 vcc, v122, v129
	s_nop 0
	s_ff1_i32_b32 s12, vcc_lo
	s_ff1_i32_b32 s14, vcc_hi
	v_sub_f32_e32 v130, v127, v126
	v_sub_f32_e32 v131, v128, v126
	v_sub_f32_e32 v132, v129, v126
	v_mul_f32_e32 v130, 0x3fb8aa3b, v130
	v_mul_f32_e32 v131, 0x3fb8aa3b, v131
	v_mul_f32_e32 v132, 0x3fb8aa3b, v132
	v_exp_f32_e32 v67, v130
	v_exp_f32_e32 v68, v131
	v_exp_f32_e32 v69, v132
	v_lshrrev_b32_e32 v125, 5, v147
	v_writelane_b32 v70, s17, 0
	v_writelane_b32 v70, s31, 32
	v_add_f32_e32 v133, 1.0, v67
	v_add_f32_e32 v133, v133, v68
	v_add_f32_e32 v133, v133, v69
	v_div_scale_f32 v134, s[18:19], v133, v133, 1.0
	v_rcp_f32_e32 v135, v134
	v_writelane_b32 v71, s29, 0
	v_writelane_b32 v71, s34, 32
	v_fma_f32 v136, -v134, v135, 1.0
	v_fmac_f32_e32 v135, v136, v135
	v_div_scale_f32 v136, vcc, 1.0, v133, 1.0
	v_mul_f32_e32 v137, v136, v135
	v_fma_f32 v130, -v134, v137, v136
	v_fmac_f32_e32 v137, v130, v135
	v_fma_f32 v134, -v134, v137, v136
	v_div_fmas_f32 v134, v134, v135, v137
	v_writelane_b32 v72, s30, 0
	v_writelane_b32 v72, s35, 32
	v_writelane_b32 v73, s12, 0
	v_writelane_b32 v73, s14, 32
	v_div_fixup_f32 v66, v134, v133, 1.0
	v_mul_f32_e32 v67, v67, v66
	v_mul_f32_e32 v68, v68, v66
	v_mul_f32_e32 v69, v69, v66
	s_mov_b32 exec_lo, 1
	s_mov_b32 exec_hi, 1
	s_mov_b32 s13, 0x20000
	v_or_b32_e32 v153, s16, v125
	v_lshl_add_u32 v130, v70, 2, s13
	v_lshl_add_u32 v131, v71, 2, s13
	v_lshl_add_u32 v132, v72, 2, s13
	v_lshl_add_u32 v133, v73, 2, s13
	ds_add_u32 v130, v205
	ds_add_u32 v131, v205
	ds_add_u32 v132, v205
	ds_add_u32 v133, v205
	s_mov_b64 exec, -1
	s_add_i32 s26, s26, 16
	s_cmp_eq_u32 s21, s27
	s_cbranch_scc1 .LBB0_1554
	v_mov_b64_e32 v[136:137], v[112:113]
	v_mov_b64_e32 v[128:129], v[108:109]
	v_mov_b64_e32 v[132:133], v[120:121]
	v_mov_b64_e32 v[124:125], v[116:117]
	v_mov_b64_e32 v[134:135], v[110:111]
	v_mov_b64_e32 v[126:127], v[106:107]
	v_mov_b64_e32 v[130:131], v[118:119]
	v_mov_b64_e32 v[122:123], v[114:115]
	s_branch .LBB0_1543
